# v30: v25 + spatial gating row statistics read coalesced (8 lanes per 128-byte row) and reduced with DPP adds
# speedup vs baseline: 1.0061x; 1.0061x over previous
; __device__ __forceinline__ void sg_phase(const Frame& F, const KArgs& a, const int u_first, const int u_count) {
;     ...
;         f32x4 zst[8];
;         if (tid < 128) { const f32x4* p = (const f32x4*)(ZST + (size_t)(t0 + tid) * 32);
; #pragma unroll
;             for (int i = 0; i < 8; ++i) zst[i] = p[i]; }
;         const int s_ = tid >> 2, c0 = (tid & 3) * 32; const bf16* src = ZV + (size_t)(t0 + s_) * SGW + g * 128 + c0;
.LBB0_804:
	s_and_b32 s76, s90, 0xffffff80
	s_and_saveexec_b64 s[70:71], s[2:3]
	s_cbranch_execz .LBB0_806
	v_lshrrev_b32_e32 v2, 3, v0
	v_and_b32_e32 v2, 7, v2
	v_and_b32_e32 v3, 64, v0
	v_or3_b32 v2, v2, v3, s76
	v_mov_b32_e32 v3, 0
	v_lshlrev_b64 v[2:3], 7, v[2:3]
	v_lshl_add_u64 v[18:19], s[84:85], 0, v[2:3]
	v_and_b32_e32 v2, 7, v0
	v_lshlrev_b32_e32 v2, 4, v2
	v_mov_b32_e32 v3, 0
	v_lshl_add_u64 v[18:19], v[18:19], 0, v[2:3]
	v_add_co_u32_e32 v34, vcc, 0x1000, v18
	s_nop 1
	v_addc_co_u32_e32 v35, vcc, 0, v19, vcc
	global_load_dwordx4 v[2:5], v[18:19], off
	global_load_dwordx4 v[6:9], v[18:19], off offset:1024
	global_load_dwordx4 v[10:13], v[18:19], off offset:2048
	global_load_dwordx4 v[14:17], v[18:19], off offset:3072
	global_load_dwordx4 v[22:25], v[34:35], off offset:1024
	global_load_dwordx4 v[26:29], v[34:35], off offset:2048
	global_load_dwordx4 v[30:33], v[34:35], off offset:3072
	s_nop 0
	global_load_dwordx4 v[18:21], v[34:35], off

; __device__ __forceinline__ void sg_phase(const Frame& F, const KArgs& a, const int u_first, const int u_count) {
;     ...
;         for (int j = 0; j < 8; ++j) uraw[j] = *(const u32x2*)(ZU + (size_t)(t0 + t) * SGW + g * 128 + 16 * j + 4 * kq);
;         const float bs = b_sp[g * 128 + t];
;         if (tid < 128) { float S = 0.f, Q = 0.f;
; #pragma unroll
;             for (int i = 0; i < 8; ++i) { const f32x4 v = zst[i]; S += v[0] + v[2]; Q += v[1] + v[3]; }
;             const float mu = S * (1.f / SGW), var = fmaxf(Q * (1.f / SGW) - mu * mu, 0.f); st[tid] = (f32x2){mu, rsqrtf(var + LN_EPS)}; }
.LBB0_812:
	v_add_u32_e32 v174, s76, v176
	v_ashrrev_i32_e32 v175, 31, v174
	v_lshlrev_b64 v[158:159], 11, v[174:175]
	v_lshl_add_u64 v[158:159], s[0:1], 0, v[158:159]
	v_lshl_add_u64 v[158:159], v[158:159], 0, s[78:79]
	v_mov_b32_e32 v157, v147
	v_lshl_add_u64 v[158:159], v[158:159], 0, v[156:157]
	v_lshl_add_u64 v[158:159], v[158:159], 0, v[156:157]
	global_load_dwordx4 v[170:173], v[158:159], off
	global_load_dwordx4 v[166:169], v[158:159], off offset:64
	global_load_dwordx4 v[162:165], v[158:159], off offset:128
	s_nop 0
	global_load_dwordx4 v[158:161], v[158:159], off offset:192
	v_readlane_b32 s36, v252, 47
	v_readlane_b32 s37, v252, 48
	v_readlane_b32 s38, v252, 49
	v_readlane_b32 s39, v252, 50
	v_lshl_add_u64 v[184:185], v[146:147], 2, s[36:37]
	global_load_dword v146, v[184:185], off
	v_readlane_b32 s40, v252, 51
	v_readlane_b32 s41, v252, 52
	v_readlane_b32 s42, v252, 53
	v_readlane_b32 s43, v252, 54
	v_readlane_b32 s44, v252, 55
	v_readlane_b32 s45, v252, 56
	v_readlane_b32 s46, v252, 57
	v_readlane_b32 s47, v252, 58
	v_readlane_b32 s48, v252, 59
	v_readlane_b32 s49, v252, 60
	v_readlane_b32 s50, v252, 61
	v_readlane_b32 s51, v252, 62
	s_and_saveexec_b64 s[76:77], s[2:3]
	s_cbranch_execz .LBB0_814
	s_waitcnt vmcnt(13)
	s_mov_b32 s92, 0x3a800000
	v_pk_add_f32 v[2:3], v[2:3], v[4:5]
	v_pk_add_f32 v[6:7], v[6:7], v[8:9]
	v_pk_add_f32 v[10:11], v[10:11], v[12:13]
	v_pk_add_f32 v[14:15], v[14:15], v[16:17]
	v_pk_add_f32 v[18:19], v[18:19], v[20:21]
	v_pk_add_f32 v[22:23], v[22:23], v[24:25]
	v_pk_add_f32 v[26:27], v[26:27], v[28:29]
	v_pk_add_f32 v[30:31], v[30:31], v[32:33]
	s_nop 1
	v_add_f32_dpp v2, v2, v2 quad_perm:[1,0,3,2] row_mask:0xf bank_mask:0xf
	v_add_f32_dpp v3, v3, v3 quad_perm:[1,0,3,2] row_mask:0xf bank_mask:0xf
	v_add_f32_dpp v6, v6, v6 quad_perm:[1,0,3,2] row_mask:0xf bank_mask:0xf
	v_add_f32_dpp v7, v7, v7 quad_perm:[1,0,3,2] row_mask:0xf bank_mask:0xf
	v_add_f32_dpp v10, v10, v10 quad_perm:[1,0,3,2] row_mask:0xf bank_mask:0xf
	v_add_f32_dpp v11, v11, v11 quad_perm:[1,0,3,2] row_mask:0xf bank_mask:0xf
	v_add_f32_dpp v14, v14, v14 quad_perm:[1,0,3,2] row_mask:0xf bank_mask:0xf
	v_add_f32_dpp v15, v15, v15 quad_perm:[1,0,3,2] row_mask:0xf bank_mask:0xf
	v_add_f32_dpp v18, v18, v18 quad_perm:[1,0,3,2] row_mask:0xf bank_mask:0xf
	v_add_f32_dpp v19, v19, v19 quad_perm:[1,0,3,2] row_mask:0xf bank_mask:0xf
	v_add_f32_dpp v22, v22, v22 quad_perm:[1,0,3,2] row_mask:0xf bank_mask:0xf
	v_add_f32_dpp v23, v23, v23 quad_perm:[1,0,3,2] row_mask:0xf bank_mask:0xf
	v_add_f32_dpp v26, v26, v26 quad_perm:[1,0,3,2] row_mask:0xf bank_mask:0xf
	v_add_f32_dpp v27, v27, v27 quad_perm:[1,0,3,2] row_mask:0xf bank_mask:0xf
	v_add_f32_dpp v30, v30, v30 quad_perm:[1,0,3,2] row_mask:0xf bank_mask:0xf
	v_add_f32_dpp v31, v31, v31 quad_perm:[1,0,3,2] row_mask:0xf bank_mask:0xf
	v_add_f32_dpp v2, v2, v2 quad_perm:[2,3,0,1] row_mask:0xf bank_mask:0xf
	v_add_f32_dpp v3, v3, v3 quad_perm:[2,3,0,1] row_mask:0xf bank_mask:0xf
	v_add_f32_dpp v6, v6, v6 quad_perm:[2,3,0,1] row_mask:0xf bank_mask:0xf
	v_add_f32_dpp v7, v7, v7 quad_perm:[2,3,0,1] row_mask:0xf bank_mask:0xf
	v_add_f32_dpp v10, v10, v10 quad_perm:[2,3,0,1] row_mask:0xf bank_mask:0xf
	v_add_f32_dpp v11, v11, v11 quad_perm:[2,3,0,1] row_mask:0xf bank_mask:0xf
	v_add_f32_dpp v14, v14, v14 quad_perm:[2,3,0,1] row_mask:0xf bank_mask:0xf
	v_add_f32_dpp v15, v15, v15 quad_perm:[2,3,0,1] row_mask:0xf bank_mask:0xf
	v_add_f32_dpp v18, v18, v18 quad_perm:[2,3,0,1] row_mask:0xf bank_mask:0xf
	v_add_f32_dpp v19, v19, v19 quad_perm:[2,3,0,1] row_mask:0xf bank_mask:0xf
	v_add_f32_dpp v22, v22, v22 quad_perm:[2,3,0,1] row_mask:0xf bank_mask:0xf
	v_add_f32_dpp v23, v23, v23 quad_perm:[2,3,0,1] row_mask:0xf bank_mask:0xf
	v_add_f32_dpp v26, v26, v26 quad_perm:[2,3,0,1] row_mask:0xf bank_mask:0xf
	v_add_f32_dpp v27, v27, v27 quad_perm:[2,3,0,1] row_mask:0xf bank_mask:0xf
	v_add_f32_dpp v30, v30, v30 quad_perm:[2,3,0,1] row_mask:0xf bank_mask:0xf
	v_add_f32_dpp v31, v31, v31 quad_perm:[2,3,0,1] row_mask:0xf bank_mask:0xf
	v_add_f32_dpp v2, v2, v2 row_half_mirror row_mask:0xf bank_mask:0xf
	v_add_f32_dpp v3, v3, v3 row_half_mirror row_mask:0xf bank_mask:0xf
	v_add_f32_dpp v6, v6, v6 row_half_mirror row_mask:0xf bank_mask:0xf
	v_add_f32_dpp v7, v7, v7 row_half_mirror row_mask:0xf bank_mask:0xf
	v_add_f32_dpp v10, v10, v10 row_half_mirror row_mask:0xf bank_mask:0xf
	v_add_f32_dpp v11, v11, v11 row_half_mirror row_mask:0xf bank_mask:0xf
	v_add_f32_dpp v14, v14, v14 row_half_mirror row_mask:0xf bank_mask:0xf
	v_add_f32_dpp v15, v15, v15 row_half_mirror row_mask:0xf bank_mask:0xf
	v_add_f32_dpp v18, v18, v18 row_half_mirror row_mask:0xf bank_mask:0xf
	v_add_f32_dpp v19, v19, v19 row_half_mirror row_mask:0xf bank_mask:0xf
	v_add_f32_dpp v22, v22, v22 row_half_mirror row_mask:0xf bank_mask:0xf
	v_add_f32_dpp v23, v23, v23 row_half_mirror row_mask:0xf bank_mask:0xf
	v_add_f32_dpp v26, v26, v26 row_half_mirror row_mask:0xf bank_mask:0xf
	v_add_f32_dpp v27, v27, v27 row_half_mirror row_mask:0xf bank_mask:0xf
	v_add_f32_dpp v30, v30, v30 row_half_mirror row_mask:0xf bank_mask:0xf
	v_add_f32_dpp v31, v31, v31 row_half_mirror row_mask:0xf bank_mask:0xf
	v_lshrrev_b32_e32 v186, 3, v0
	v_and_b32_e32 v186, 7, v186
	v_and_b32_e32 v187, 64, v0
	v_or_b32_e32 v186, v186, v187
	v_lshlrev_b32_e32 v186, 3, v186
	v_pk_mul_f32 v[2:3], v[2:3], s[92:93] op_sel_hi:[1,0]
	v_pk_mul_f32 v[6:7], v[6:7], s[92:93] op_sel_hi:[1,0]
	v_pk_mul_f32 v[10:11], v[10:11], s[92:93] op_sel_hi:[1,0]
	v_pk_mul_f32 v[14:15], v[14:15], s[92:93] op_sel_hi:[1,0]
	v_pk_mul_f32 v[18:19], v[18:19], s[92:93] op_sel_hi:[1,0]
	v_pk_mul_f32 v[22:23], v[22:23], s[92:93] op_sel_hi:[1,0]
	v_pk_mul_f32 v[26:27], v[26:27], s[92:93] op_sel_hi:[1,0]
	v_pk_mul_f32 v[30:31], v[30:31], s[92:93] op_sel_hi:[1,0]
	v_fma_f32 v4, -v2, v2, v3
	v_fma_f32 v8, -v6, v6, v7
	v_fma_f32 v12, -v10, v10, v11
	v_fma_f32 v16, -v14, v14, v15
	v_fma_f32 v20, -v18, v18, v19
	v_fma_f32 v24, -v22, v22, v23
	v_fma_f32 v28, -v26, v26, v27
	v_fma_f32 v32, -v30, v30, v31
	v_max_f32_e32 v4, 0, v4
	v_max_f32_e32 v8, 0, v8
	v_max_f32_e32 v12, 0, v12
	v_max_f32_e32 v16, 0, v16
	v_max_f32_e32 v20, 0, v20
	v_max_f32_e32 v24, 0, v24
	v_max_f32_e32 v28, 0, v28
	v_max_f32_e32 v32, 0, v32
	v_add_f32_e32 v4, 0x3727c5ac, v4
	v_add_f32_e32 v8, 0x3727c5ac, v8
	v_add_f32_e32 v12, 0x3727c5ac, v12
	v_add_f32_e32 v16, 0x3727c5ac, v16
	v_add_f32_e32 v20, 0x3727c5ac, v20
	v_add_f32_e32 v24, 0x3727c5ac, v24
	v_add_f32_e32 v28, 0x3727c5ac, v28
	v_add_f32_e32 v32, 0x3727c5ac, v32
	v_rsq_f32_e32 v3, v4
	v_rsq_f32_e32 v7, v8
	v_rsq_f32_e32 v11, v12
	v_rsq_f32_e32 v15, v16
	v_rsq_f32_e32 v19, v20
	v_rsq_f32_e32 v23, v24
	v_rsq_f32_e32 v27, v28
	v_rsq_f32_e32 v31, v32
	s_nop 0
	ds_write_b64 v186, v[2:3]
	ds_write_b64 v186, v[6:7] offset:64
	ds_write_b64 v186, v[10:11] offset:128
	ds_write_b64 v186, v[14:15] offset:192
	ds_write_b64 v186, v[18:19] offset:256
	ds_write_b64 v186, v[22:23] offset:320
	ds_write_b64 v186, v[26:27] offset:384
	ds_write_b64 v186, v[30:31] offset:448
